# node0 input projection moved from VALU f32 FMAs to v_mfma_f32_32x32x2_f32 (f32 operands, transposed tiles + permlane32 swap), 3 waves per SIMD
# speedup vs baseline: 1.0139x; 1.0112x over previous
_Z14k_bcount_node0ItEvPKiPiS2_PKfS4_S4_S4_PK15HIP_vector_typeIjLj4EEPtPT_SB_:
	s_cmpk_gt_u32 s2, 0xf4
	s_mov_b64 s[4:5], -1
	s_cbranch_scc0 .LBB5_8
	s_load_dwordx2 s[8:9], s[0:1], 0x20
	s_load_dwordx2 s[6:7], s[0:1], 0x38
	s_load_dwordx2 s[20:21], s[0:1], 0x18
	s_load_dword s22, s[0:1], 0x58
	v_mov_b32_e32 v3, 0
	v_lshlrev_b32_e32 v2, 4, v0
	v_cmp_gt_u32_e64 s[4:5], 16, v0
	s_waitcnt lgkmcnt(0)
	v_lshl_add_u64 v[4:5], s[8:9], 0, v[2:3]
	v_mov_b32_e32 v6, v3
	v_mov_b32_e32 v7, v3
	v_mov_b32_e32 v8, v3
	v_mov_b32_e32 v9, v3
	s_and_saveexec_b64 s[8:9], s[4:5]
	s_cbranch_execz .LBB5_3
	v_add_co_u32_e32 v6, vcc, 0x3000, v4
	s_nop 1
	v_addc_co_u32_e32 v7, vcc, 0, v5, vcc
	global_load_dwordx4 v[6:9], v[6:7], off
.LBB5_3:
	s_or_b64 exec, exec, s[8:9]
	v_lshl_add_u64 v[38:39], s[6:7], 0, v[2:3]
	v_add_co_u32_e32 v30, vcc, 0x1000, v38
	v_or_b32_e32 v1, 0x4000, v2
	s_nop 0
	v_addc_co_u32_e32 v31, vcc, 0, v39, vcc
	v_add_co_u32_e32 v32, vcc, 0x2000, v38
	global_load_dwordx4 v[10:13], v2, s[6:7]
	s_nop 0
	v_addc_co_u32_e32 v33, vcc, 0, v39, vcc
	v_add_co_u32_e32 v34, vcc, 0x3000, v38
	s_nop 1
	v_addc_co_u32_e32 v35, vcc, 0, v39, vcc
	v_add_co_u32_e32 v40, vcc, 0x5000, v38
	global_load_dwordx4 v[14:17], v[32:33], off
	global_load_dwordx4 v[18:21], v[34:35], off
	global_load_dwordx4 v[22:25], v[30:31], off
	global_load_dwordx4 v[26:29], v1, s[6:7]
	v_addc_co_u32_e32 v41, vcc, 0, v39, vcc
	v_add_co_u32_e32 v42, vcc, 0x6000, v38
	s_nop 1
	v_addc_co_u32_e32 v43, vcc, 0, v39, vcc
	v_add_co_u32_e32 v46, vcc, 0x7000, v38
	global_load_dwordx4 v[30:33], v[40:41], off
	global_load_dwordx4 v[34:37], v[42:43], off
	v_addc_co_u32_e32 v47, vcc, 0, v39, vcc
	v_add_co_u32_e32 v54, vcc, 0x1000, v4
	global_load_dwordx4 v[38:41], v[46:47], off
	global_load_dwordx4 v[42:45], v[4:5], off
	v_addc_co_u32_e32 v55, vcc, 0, v5, vcc
	v_add_co_u32_e32 v4, vcc, 0x2000, v4
	s_nop 1
	v_addc_co_u32_e32 v5, vcc, 0, v5, vcc
	global_load_dwordx4 v[46:49], v[54:55], off
	global_load_dwordx4 v[50:53], v[4:5], off
	s_load_dword s3, s[0:1], 0x58
	s_waitcnt vmcnt(10)
	ds_write_b128 v2, v[10:13]
	s_waitcnt vmcnt(7)
	ds_write_b128 v2, v[22:25] offset:4096
	s_waitcnt vmcnt(6)
	ds_write_b128 v2, v[26:29] offset:16384
	ds_write_b128 v2, v[14:17] offset:8192
	ds_write_b128 v2, v[18:21] offset:12288
	s_waitcnt vmcnt(5)
	ds_write_b128 v2, v[30:33] offset:20480
	s_waitcnt vmcnt(4)
	ds_write_b128 v2, v[34:37] offset:24576
	s_waitcnt vmcnt(3)
	ds_write_b128 v2, v[38:41] offset:28672
	s_waitcnt vmcnt(2)
	ds_write_b128 v2, v[42:45] offset:32768
	s_waitcnt vmcnt(1)
	ds_write_b128 v2, v[46:49] offset:36864
	s_waitcnt vmcnt(0)
	ds_write_b128 v2, v[50:53] offset:40960
	s_and_saveexec_b64 s[6:7], s[4:5]
	ds_write_b128 v2, v[6:9] offset:45056
	s_or_b64 exec, exec, s[6:7]
	s_add_i32 s22, s22, 0xffffff0b
	s_add_i32 s23, s2, 0xffffff0b
	v_lshrrev_b32_e32 v101, 6, v0
	v_mul_lo_u32 v101, s22, v101
	v_add_u32_e32 v101, s23, v101
	v_min_u32_e32 v101, 0xc34, v101
	v_and_b32_e32 v102, 31, v0
	v_lshl_or_b32 v101, v101, 5, v102
	v_mul_u32_u24_e32 v101, 0xc4, v101
	global_load_dwordx4 v[52:55], v101, s[20:21]
	global_load_dwordx4 v[56:59], v101, s[20:21] offset:16
	global_load_dwordx4 v[60:63], v101, s[20:21] offset:32
	global_load_dwordx4 v[64:67], v101, s[20:21] offset:48
	global_load_dwordx4 v[68:71], v101, s[20:21] offset:64
	global_load_dwordx4 v[72:75], v101, s[20:21] offset:80
	global_load_dwordx4 v[76:79], v101, s[20:21] offset:96
	global_load_dwordx4 v[80:83], v101, s[20:21] offset:112
	global_load_dwordx4 v[84:87], v101, s[20:21] offset:128
	global_load_dwordx4 v[88:91], v101, s[20:21] offset:144
	global_load_dwordx4 v[92:95], v101, s[20:21] offset:160
	global_load_dwordx4 v[96:99], v101, s[20:21] offset:176
	global_load_dword v100, v101, s[20:21] offset:192
	s_waitcnt lgkmcnt(0)
	s_addk_i32 s3, 0xff0b
	v_lshrrev_b32_e32 v1, 6, v0
	s_add_i32 s4, s2, 0xffffff0b
	v_mul_lo_u32 v1, s3, v1
	v_add_u32_e32 v1, s4, v1
	s_movk_i32 s3, 0xc35
	v_cmp_gt_i32_e32 vcc, s3, v1
	s_barrier
	s_and_saveexec_b64 s[8:9], vcc
	s_cbranch_execz .LBB5_7
	s_load_dwordx2 s[24:25], s[0:1], 0x28
	s_load_dwordx2 s[4:5], s[0:1], 0x30
	s_load_dwordx2 s[26:27], s[0:1], 0x40
	s_load_dwordx2 s[6:7], s[0:1], 0x48
	s_load_dwordx2 s[2:3], s[0:1], 0x50
	v_and_b32_e32 v14, 32, v0
	v_and_b32_e32 v15, 31, v0
	v_cmp_ne_u32_e32 vcc, 0, v14
	v_lshrrev_b32_e32 v16, 1, v14
	v_lshlrev_b32_e32 v17, 3, v14
	v_lshl_add_u32 v17, v15, 2, v17
	v_lshlrev_b32_e32 v15, 2, v15
	v_mov_b32_e32 v13, 0
	s_waitcnt lgkmcnt(0)
	global_load_dwordx4 v[20:23], v16, s[24:25]
	global_load_dwordx4 v[24:27], v16, s[24:25] offset:32
	global_load_dwordx4 v[28:31], v16, s[24:25] offset:64
	global_load_dwordx4 v[32:35], v16, s[24:25] offset:96
	global_load_dwordx4 v[36:39], v16, s[24:25] offset:128
	global_load_dwordx4 v[40:43], v16, s[24:25] offset:160
	global_load_dwordx4 v[44:47], v16, s[24:25] offset:192
	global_load_dwordx4 v[48:51], v16, s[24:25] offset:224
	ds_read_b32 v2, v17 offset:32768
	ds_read_b32 v3, v17 offset:32896
	ds_read_b32 v4, v17 offset:33280
	ds_read_b32 v5, v17 offset:33408
	ds_read_b32 v6, v17 offset:33792
	ds_read_b32 v7, v17 offset:33920
	ds_read_b32 v8, v17 offset:34304
	ds_read_b32 v9, v17 offset:34432
	s_waitcnt vmcnt(8)
	v_cndmask_b32_e32 v10, v52, v53, vcc
	s_waitcnt vmcnt(0)
	v_cndmask_b32_e32 v11, v54, v55, vcc
	s_waitcnt lgkmcnt(6)
	v_mfma_f32_32x32x2_f32 v[20:35], v2, v10, v[20:35]
	v_mfma_f32_32x32x2_f32 v[36:51], v3, v10, v[36:51]
	ds_read_b32 v2, v17 offset:34816
	ds_read_b32 v3, v17 offset:34944
	v_cndmask_b32_e32 v12, v56, v57, vcc
	s_waitcnt lgkmcnt(6)
	v_mfma_f32_32x32x2_f32 v[20:35], v4, v11, v[20:35]
	v_mfma_f32_32x32x2_f32 v[36:51], v5, v11, v[36:51]
	ds_read_b32 v4, v17 offset:35328
	ds_read_b32 v5, v17 offset:35456
	v_cndmask_b32_e32 v10, v58, v59, vcc
	s_waitcnt lgkmcnt(6)
	v_mfma_f32_32x32x2_f32 v[20:35], v6, v12, v[20:35]
	v_mfma_f32_32x32x2_f32 v[36:51], v7, v12, v[36:51]
	ds_read_b32 v6, v17 offset:35840
	ds_read_b32 v7, v17 offset:35968
	v_cndmask_b32_e32 v11, v60, v61, vcc
	s_waitcnt lgkmcnt(6)
	v_mfma_f32_32x32x2_f32 v[20:35], v8, v10, v[20:35]
	v_mfma_f32_32x32x2_f32 v[36:51], v9, v10, v[36:51]
	ds_read_b32 v8, v17 offset:36352
	ds_read_b32 v9, v17 offset:36480
	v_cndmask_b32_e32 v12, v62, v63, vcc
	s_waitcnt lgkmcnt(6)
	v_mfma_f32_32x32x2_f32 v[20:35], v2, v11, v[20:35]
	v_mfma_f32_32x32x2_f32 v[36:51], v3, v11, v[36:51]
	ds_read_b32 v2, v17 offset:36864
	ds_read_b32 v3, v17 offset:36992
	v_cndmask_b32_e32 v10, v64, v65, vcc
	s_waitcnt lgkmcnt(6)
	v_mfma_f32_32x32x2_f32 v[20:35], v4, v12, v[20:35]
	v_mfma_f32_32x32x2_f32 v[36:51], v5, v12, v[36:51]
	ds_read_b32 v4, v17 offset:37376
	ds_read_b32 v5, v17 offset:37504
	v_cndmask_b32_e32 v11, v66, v67, vcc
	s_waitcnt lgkmcnt(6)
	v_mfma_f32_32x32x2_f32 v[20:35], v6, v10, v[20:35]
	v_mfma_f32_32x32x2_f32 v[36:51], v7, v10, v[36:51]
	ds_read_b32 v6, v17 offset:37888
	ds_read_b32 v7, v17 offset:38016
	v_cndmask_b32_e32 v12, v68, v69, vcc
	s_waitcnt lgkmcnt(6)
	v_mfma_f32_32x32x2_f32 v[20:35], v8, v11, v[20:35]
	v_mfma_f32_32x32x2_f32 v[36:51], v9, v11, v[36:51]
	ds_read_b32 v8, v17 offset:38400
	ds_read_b32 v9, v17 offset:38528
	v_cndmask_b32_e32 v10, v70, v71, vcc
	s_waitcnt lgkmcnt(6)
	v_mfma_f32_32x32x2_f32 v[20:35], v2, v12, v[20:35]
	v_mfma_f32_32x32x2_f32 v[36:51], v3, v12, v[36:51]
	ds_read_b32 v2, v17 offset:38912
	ds_read_b32 v3, v17 offset:39040
	v_cndmask_b32_e32 v11, v72, v73, vcc
	s_waitcnt lgkmcnt(6)
	v_mfma_f32_32x32x2_f32 v[20:35], v4, v10, v[20:35]
	v_mfma_f32_32x32x2_f32 v[36:51], v5, v10, v[36:51]
	ds_read_b32 v4, v17 offset:39424
	ds_read_b32 v5, v17 offset:39552
	v_cndmask_b32_e32 v12, v74, v75, vcc
	s_waitcnt lgkmcnt(6)
	v_mfma_f32_32x32x2_f32 v[20:35], v6, v11, v[20:35]
	v_mfma_f32_32x32x2_f32 v[36:51], v7, v11, v[36:51]
	ds_read_b32 v6, v17 offset:39936
	ds_read_b32 v7, v17 offset:40064
	v_cndmask_b32_e32 v10, v76, v77, vcc
	s_waitcnt lgkmcnt(6)
	v_mfma_f32_32x32x2_f32 v[20:35], v8, v12, v[20:35]
	v_mfma_f32_32x32x2_f32 v[36:51], v9, v12, v[36:51]
	ds_read_b32 v8, v17 offset:40448
	ds_read_b32 v9, v17 offset:40576
	v_cndmask_b32_e32 v11, v78, v79, vcc
	s_waitcnt lgkmcnt(6)
	v_mfma_f32_32x32x2_f32 v[20:35], v2, v10, v[20:35]
	v_mfma_f32_32x32x2_f32 v[36:51], v3, v10, v[36:51]
	ds_read_b32 v2, v17 offset:40960
	ds_read_b32 v3, v17 offset:41088
	v_cndmask_b32_e32 v12, v80, v81, vcc
	s_waitcnt lgkmcnt(6)
	v_mfma_f32_32x32x2_f32 v[20:35], v4, v11, v[20:35]
	v_mfma_f32_32x32x2_f32 v[36:51], v5, v11, v[36:51]
	ds_read_b32 v4, v17 offset:41472
	ds_read_b32 v5, v17 offset:41600
	v_cndmask_b32_e32 v10, v82, v83, vcc
	s_waitcnt lgkmcnt(6)
	v_mfma_f32_32x32x2_f32 v[20:35], v6, v12, v[20:35]
	v_mfma_f32_32x32x2_f32 v[36:51], v7, v12, v[36:51]
	ds_read_b32 v6, v17 offset:41984
	ds_read_b32 v7, v17 offset:42112
	v_cndmask_b32_e32 v11, v84, v85, vcc
	s_waitcnt lgkmcnt(6)
	v_mfma_f32_32x32x2_f32 v[20:35], v8, v10, v[20:35]
	v_mfma_f32_32x32x2_f32 v[36:51], v9, v10, v[36:51]
	ds_read_b32 v8, v17 offset:42496
	ds_read_b32 v9, v17 offset:42624
	v_cndmask_b32_e32 v12, v86, v87, vcc
	s_waitcnt lgkmcnt(6)
	v_mfma_f32_32x32x2_f32 v[20:35], v2, v11, v[20:35]
	v_mfma_f32_32x32x2_f32 v[36:51], v3, v11, v[36:51]
	ds_read_b32 v2, v17 offset:43008
	ds_read_b32 v3, v17 offset:43136
	v_cndmask_b32_e32 v10, v88, v89, vcc
	s_waitcnt lgkmcnt(6)
	v_mfma_f32_32x32x2_f32 v[20:35], v4, v12, v[20:35]
	v_mfma_f32_32x32x2_f32 v[36:51], v5, v12, v[36:51]
	ds_read_b32 v4, v17 offset:43520
	ds_read_b32 v5, v17 offset:43648
	v_cndmask_b32_e32 v11, v90, v91, vcc
	s_waitcnt lgkmcnt(6)
	v_mfma_f32_32x32x2_f32 v[20:35], v6, v10, v[20:35]
	v_mfma_f32_32x32x2_f32 v[36:51], v7, v10, v[36:51]
	ds_read_b32 v6, v17 offset:44032
	ds_read_b32 v7, v17 offset:44160
	v_cndmask_b32_e32 v12, v92, v93, vcc
	s_waitcnt lgkmcnt(6)
	v_mfma_f32_32x32x2_f32 v[20:35], v8, v11, v[20:35]
	v_mfma_f32_32x32x2_f32 v[36:51], v9, v11, v[36:51]
	ds_read_b32 v8, v17 offset:44544
	ds_read_b32 v9, v17 offset:44672
	v_cndmask_b32_e32 v10, v94, v95, vcc
	s_waitcnt lgkmcnt(6)
	v_mfma_f32_32x32x2_f32 v[20:35], v2, v12, v[20:35]
	v_mfma_f32_32x32x2_f32 v[36:51], v3, v12, v[36:51]
	ds_read_b32 v2, v15 offset:45056
	ds_read_b32 v3, v15 offset:45184
	v_cndmask_b32_e32 v11, v96, v97, vcc
	s_waitcnt lgkmcnt(6)
	v_mfma_f32_32x32x2_f32 v[20:35], v4, v10, v[20:35]
	v_mfma_f32_32x32x2_f32 v[36:51], v5, v10, v[36:51]
	v_cndmask_b32_e32 v12, v98, v99, vcc
	s_waitcnt lgkmcnt(4)
	v_mfma_f32_32x32x2_f32 v[20:35], v6, v11, v[20:35]
	v_mfma_f32_32x32x2_f32 v[36:51], v7, v11, v[36:51]
	v_cndmask_b32_e32 v10, v100, v13, vcc
	s_waitcnt lgkmcnt(2)
	v_mfma_f32_32x32x2_f32 v[20:35], v8, v12, v[20:35]
	v_mfma_f32_32x32x2_f32 v[36:51], v9, v12, v[36:51]
	s_waitcnt lgkmcnt(0)
	v_mfma_f32_32x32x2_f32 v[20:35], v2, v10, v[20:35]
	v_mfma_f32_32x32x2_f32 v[36:51], v3, v10, v[36:51]
	s_nop 15
	s_nop 3
	v_permlane32_swap_b32_e32 v20, v36
	v_permlane32_swap_b32_e32 v21, v37
	v_permlane32_swap_b32_e32 v22, v38
	v_permlane32_swap_b32_e32 v23, v39
	v_permlane32_swap_b32_e32 v24, v40
	v_permlane32_swap_b32_e32 v25, v41
	v_permlane32_swap_b32_e32 v26, v42
	v_permlane32_swap_b32_e32 v27, v43
	v_permlane32_swap_b32_e32 v28, v44
	v_permlane32_swap_b32_e32 v29, v45
	v_permlane32_swap_b32_e32 v30, v46
	v_permlane32_swap_b32_e32 v31, v47
	v_permlane32_swap_b32_e32 v32, v48
	v_permlane32_swap_b32_e32 v33, v49
	v_permlane32_swap_b32_e32 v34, v50
	v_permlane32_swap_b32_e32 v35, v51
	v_cvt_pk_f16_f32 v14, v20, v21
	v_cvt_pk_f16_f32 v15, v22, v23
	v_cvt_pk_f16_f32 v16, v36, v37
	v_cvt_pk_f16_f32 v17, v38, v39
	v_cvt_pk_f16_f32 v10, v24, v25
	v_cvt_pk_f16_f32 v11, v26, v27
	v_cvt_pk_f16_f32 v12, v40, v41
	v_cvt_pk_f16_f32 v13, v42, v43
	v_cvt_pk_f16_f32 v6, v28, v29
	v_cvt_pk_f16_f32 v7, v30, v31
	v_cvt_pk_f16_f32 v8, v44, v45
	v_cvt_pk_f16_f32 v9, v46, v47
	v_cvt_pk_f16_f32 v2, v32, v33
	v_cvt_pk_f16_f32 v3, v34, v35
	v_cvt_pk_f16_f32 v4, v48, v49
	v_cvt_pk_f16_f32 v5, v50, v51
	v_and_b32_e32 v22, 31, v0
	v_and_b32_e32 v23, 63, v0
	v_lshlrev_b32_e32 v23, 4, v23
	v_and_b32_e32 v24, 32, v0
	v_lshlrev_b32_e32 v25, 5, v1
	v_or_b32_e32 v20, v25, v22
	v_lshlrev_b32_e32 v20, 7, v20
	v_lshl_add_u32 v20, v24, 1, v20
	v_mov_b32_e32 v21, 0
	v_lshl_add_u64 v[18:19], s[26:27], 0, v[20:21]
	v_lshrrev_b32_e32 v24, 3, v24
	v_or_b32_e32 v0, v25, v24
	v_mov_b32_e32 v1, 0
	global_store_dwordx4 v[18:19], v[14:17], off
	global_store_dwordx4 v[18:19], v[10:13], off offset:16
	global_store_dwordx4 v[18:19], v[6:9], off offset:32
	global_store_dwordx4 v[18:19], v[2:5], off offset:48
	v_lshlrev_b32_e32 v18, 3, v22
	global_load_dwordx2 a[0:1], v18, s[4:5]
	ds_read_b128 v[18:21], v23
	ds_read_b128 v[24:27], v23 offset:8192
	ds_read_b128 v[28:31], v23 offset:4096
	ds_read_b128 v[32:35], v23 offset:12288
	s_waitcnt vmcnt(0)
	v_accvgpr_mov_b32 a16, a0
	v_accvgpr_mov_b32 a17, a0
	v_accvgpr_mov_b32 a18, a0
	v_accvgpr_mov_b32 a19, a0
	v_accvgpr_mov_b32 a20, a0
	v_accvgpr_mov_b32 a21, a0
	v_accvgpr_mov_b32 a22, a0
	v_accvgpr_mov_b32 a23, a0
	v_accvgpr_mov_b32 a24, a0
	v_accvgpr_mov_b32 a25, a0
	v_accvgpr_mov_b32 a26, a0
	v_accvgpr_mov_b32 a27, a0
	v_accvgpr_mov_b32 a28, a0
	v_accvgpr_mov_b32 a29, a0
	v_accvgpr_mov_b32 a30, a0
	v_accvgpr_mov_b32 a31, a0
	v_accvgpr_mov_b32 a0, a1
	v_accvgpr_mov_b32 a2, a1
	v_accvgpr_mov_b32 a3, a1
	v_accvgpr_mov_b32 a4, a1
	v_accvgpr_mov_b32 a5, a1
	v_accvgpr_mov_b32 a6, a1
	v_accvgpr_mov_b32 a7, a1
	v_accvgpr_mov_b32 a8, a1
	v_accvgpr_mov_b32 a9, a1
	v_accvgpr_mov_b32 a10, a1
	v_accvgpr_mov_b32 a11, a1
	v_accvgpr_mov_b32 a12, a1
	v_accvgpr_mov_b32 a13, a1
	v_accvgpr_mov_b32 a14, a1
	v_accvgpr_mov_b32 a15, a1
	s_waitcnt lgkmcnt(3)
	v_mfma_f32_32x32x16_f16 a[16:31], v[14:17], v[18:21], a[16:31]
	s_waitcnt lgkmcnt(1)
	v_mfma_f32_32x32x16_f16 a[0:15], v[14:17], v[28:31], a[0:15]
	v_mfma_f32_32x32x16_f16 a[16:31], v[14:17], v[24:27], a[16:31]
	s_waitcnt lgkmcnt(0)
	v_mfma_f32_32x32x16_f16 a[0:15], v[14:17], v[32:35], a[0:15]
	ds_read_b128 v[18:21], v23 offset:1024
	ds_read_b128 v[24:27], v23 offset:9216
	ds_read_b128 v[28:31], v23 offset:5120
	ds_read_b128 v[32:35], v23 offset:13312
	s_waitcnt lgkmcnt(3)
	v_mfma_f32_32x32x16_f16 a[16:31], v[10:13], v[18:21], a[16:31]
	s_waitcnt lgkmcnt(1)
	v_mfma_f32_32x32x16_f16 a[0:15], v[10:13], v[28:31], a[0:15]
	v_mfma_f32_32x32x16_f16 a[16:31], v[10:13], v[24:27], a[16:31]
	s_waitcnt lgkmcnt(0)
	v_mfma_f32_32x32x16_f16 a[0:15], v[10:13], v[32:35], a[0:15]
	ds_read_b128 v[18:21], v23 offset:2048
	ds_read_b128 v[24:27], v23 offset:10240
	ds_read_b128 v[28:31], v23 offset:6144
	ds_read_b128 v[32:35], v23 offset:14336
	s_waitcnt lgkmcnt(3)
	v_mfma_f32_32x32x16_f16 a[16:31], v[6:9], v[18:21], a[16:31]
	s_waitcnt lgkmcnt(1)
	v_mfma_f32_32x32x16_f16 a[0:15], v[6:9], v[28:31], a[0:15]
	v_mfma_f32_32x32x16_f16 a[16:31], v[6:9], v[24:27], a[16:31]
	s_waitcnt lgkmcnt(0)
	v_mfma_f32_32x32x16_f16 a[0:15], v[6:9], v[32:35], a[0:15]
	ds_read_b128 v[18:21], v23 offset:3072
	ds_read_b128 v[24:27], v23 offset:11264
	ds_read_b128 v[28:31], v23 offset:7168
	ds_read_b128 v[32:35], v23 offset:15360
	s_waitcnt lgkmcnt(3)
	v_mfma_f32_32x32x16_f16 a[16:31], v[2:5], v[18:21], a[16:31]
	s_waitcnt lgkmcnt(1)
	v_mfma_f32_32x32x16_f16 a[0:15], v[2:5], v[28:31], a[0:15]
	v_mfma_f32_32x32x16_f16 a[16:31], v[2:5], v[24:27], a[16:31]
	s_waitcnt lgkmcnt(0)
	v_mfma_f32_32x32x16_f16 a[0:15], v[2:5], v[32:35], a[0:15]
	ds_read_b128 v[18:21], v23 offset:16384
	ds_read_b128 v[24:27], v23 offset:24576
	ds_read_b128 v[28:31], v23 offset:20480
	ds_read_b128 v[32:35], v23 offset:28672
	s_waitcnt lgkmcnt(3)
	v_mfma_f32_32x32x16_f16 a[32:47], v[14:17], v[18:21], 0
	s_waitcnt lgkmcnt(1)
	v_mfma_f32_32x32x16_f16 a[48:63], v[14:17], v[28:31], 0
	v_mfma_f32_32x32x16_f16 a[32:47], v[14:17], v[24:27], a[32:47]
	s_waitcnt lgkmcnt(0)
	v_mfma_f32_32x32x16_f16 a[48:63], v[14:17], v[32:35], a[48:63]
	ds_read_b128 v[14:17], v23 offset:17408
	ds_read_b128 v[18:21], v23 offset:25600
	ds_read_b128 v[24:27], v23 offset:21504
	ds_read_b128 v[28:31], v23 offset:29696
	s_waitcnt lgkmcnt(3)
	v_mfma_f32_32x32x16_f16 a[32:47], v[10:13], v[14:17], a[32:47]
	s_waitcnt lgkmcnt(1)
	v_mfma_f32_32x32x16_f16 a[48:63], v[10:13], v[24:27], a[48:63]
	v_mfma_f32_32x32x16_f16 a[32:47], v[10:13], v[18:21], a[32:47]
	s_waitcnt lgkmcnt(0)
	v_mfma_f32_32x32x16_f16 a[48:63], v[10:13], v[28:31], a[48:63]
	ds_read_b128 v[10:13], v23 offset:18432
	ds_read_b128 v[14:17], v23 offset:26624
	ds_read_b128 v[18:21], v23 offset:22528
	ds_read_b128 v[24:27], v23 offset:30720
	s_waitcnt lgkmcnt(3)
	v_mfma_f32_32x32x16_f16 a[32:47], v[6:9], v[10:13], a[32:47]
	s_waitcnt lgkmcnt(1)
	v_mfma_f32_32x32x16_f16 a[48:63], v[6:9], v[18:21], a[48:63]
	v_mfma_f32_32x32x16_f16 a[32:47], v[6:9], v[14:17], a[32:47]
	s_waitcnt lgkmcnt(0)
	v_mfma_f32_32x32x16_f16 a[48:63], v[6:9], v[24:27], a[48:63]
	ds_read_b128 v[10:13], v23 offset:19456
	ds_read_b128 v[6:9], v23 offset:27648
	ds_read_b128 v[18:21], v23 offset:23552
	ds_read_b128 v[14:17], v23 offset:31744
	s_waitcnt lgkmcnt(3)
	v_mfma_f32_32x32x16_f16 a[32:47], v[2:5], v[10:13], a[32:47]
	s_waitcnt lgkmcnt(1)
	v_mfma_f32_32x32x16_f16 a[48:63], v[2:5], v[18:21], a[48:63]
	v_mfma_f32_32x32x16_f16 a[32:47], v[2:5], v[6:9], a[32:47]
	v_lshlrev_b32_e32 v7, 2, v22
	s_waitcnt lgkmcnt(0)
	v_mfma_f32_32x32x16_f16 a[48:63], v[2:5], v[14:17], a[48:63]
	v_accvgpr_read_b32 v2, a0
	v_accvgpr_read_b32 v3, a16
	v_cvt_pk_bf16_f32 v6, v3, v2
	v_lshlrev_b64 v[2:3], 7, v[0:1]
	v_or_b32_e32 v2, v2, v7
	v_lshl_add_u64 v[4:5], s[6:7], 0, v[2:3]
	global_store_dword v[4:5], v6, off
	s_nop 1
	v_accvgpr_read_b32 v4, a32
	v_lshl_add_u64 v[2:3], s[2:3], 0, v[2:3]
	s_nop 0
	v_accvgpr_read_b32 v1, a48
	v_cvt_pk_bf16_f32 v1, v4, v1
	global_store_dword v[2:3], v1, off
	v_or_b32_e32 v2, 1, v0
	v_ashrrev_i32_e32 v3, 31, v2
	v_lshlrev_b64 v[2:3], 7, v[2:3]
	v_accvgpr_read_b32 v1, a1
	v_accvgpr_read_b32 v4, a17
	v_or_b32_e32 v2, v2, v7
	v_cvt_pk_bf16_f32 v1, v4, v1
	v_lshl_add_u64 v[4:5], s[6:7], 0, v[2:3]
	global_store_dword v[4:5], v1, off
	v_accvgpr_read_b32 v1, a49
	v_accvgpr_read_b32 v4, a33
	v_cvt_pk_bf16_f32 v1, v4, v1
	v_lshl_add_u64 v[2:3], s[2:3], 0, v[2:3]
	global_store_dword v[2:3], v1, off
	v_or_b32_e32 v2, 2, v0
	v_ashrrev_i32_e32 v3, 31, v2
	v_lshlrev_b64 v[2:3], 7, v[2:3]
	v_accvgpr_read_b32 v1, a2
	v_accvgpr_read_b32 v4, a18
	v_or_b32_e32 v2, v2, v7
	v_cvt_pk_bf16_f32 v1, v4, v1
	v_lshl_add_u64 v[4:5], s[6:7], 0, v[2:3]
	global_store_dword v[4:5], v1, off
	v_accvgpr_read_b32 v1, a50
	v_accvgpr_read_b32 v4, a34
	v_cvt_pk_bf16_f32 v1, v4, v1
	v_lshl_add_u64 v[2:3], s[2:3], 0, v[2:3]
	global_store_dword v[2:3], v1, off
	v_or_b32_e32 v2, 3, v0
	v_ashrrev_i32_e32 v3, 31, v2
	v_lshlrev_b64 v[2:3], 7, v[2:3]
	v_accvgpr_read_b32 v1, a3
	v_accvgpr_read_b32 v4, a19
	v_or_b32_e32 v2, v2, v7
	v_cvt_pk_bf16_f32 v1, v4, v1
	v_lshl_add_u64 v[4:5], s[6:7], 0, v[2:3]
	global_store_dword v[4:5], v1, off
	v_accvgpr_read_b32 v1, a51
	v_accvgpr_read_b32 v4, a35
	v_cvt_pk_bf16_f32 v1, v4, v1
	v_lshl_add_u64 v[2:3], s[2:3], 0, v[2:3]
	global_store_dword v[2:3], v1, off
	v_or_b32_e32 v2, 8, v0
	v_ashrrev_i32_e32 v3, 31, v2
	v_lshlrev_b64 v[2:3], 7, v[2:3]
	v_accvgpr_read_b32 v1, a4
	v_accvgpr_read_b32 v4, a20
	v_or_b32_e32 v2, v2, v7
	v_cvt_pk_bf16_f32 v1, v4, v1
	v_lshl_add_u64 v[4:5], s[6:7], 0, v[2:3]
	global_store_dword v[4:5], v1, off
	v_accvgpr_read_b32 v1, a52
	v_accvgpr_read_b32 v4, a36
	v_cvt_pk_bf16_f32 v1, v4, v1
	v_lshl_add_u64 v[2:3], s[2:3], 0, v[2:3]
	global_store_dword v[2:3], v1, off
	v_or_b32_e32 v2, 9, v0
	v_ashrrev_i32_e32 v3, 31, v2
	v_lshlrev_b64 v[2:3], 7, v[2:3]
	v_accvgpr_read_b32 v1, a5
	v_accvgpr_read_b32 v4, a21
	v_or_b32_e32 v2, v2, v7
	v_cvt_pk_bf16_f32 v1, v4, v1
	v_lshl_add_u64 v[4:5], s[6:7], 0, v[2:3]
	global_store_dword v[4:5], v1, off
	v_accvgpr_read_b32 v1, a53
	v_accvgpr_read_b32 v4, a37
	v_cvt_pk_bf16_f32 v1, v4, v1
	v_lshl_add_u64 v[2:3], s[2:3], 0, v[2:3]
	global_store_dword v[2:3], v1, off
	v_or_b32_e32 v2, 10, v0
	v_ashrrev_i32_e32 v3, 31, v2
	v_lshlrev_b64 v[2:3], 7, v[2:3]
	v_accvgpr_read_b32 v1, a6
	v_accvgpr_read_b32 v4, a22
	v_or_b32_e32 v2, v2, v7
	v_cvt_pk_bf16_f32 v1, v4, v1
	v_lshl_add_u64 v[4:5], s[6:7], 0, v[2:3]
	global_store_dword v[4:5], v1, off
	v_accvgpr_read_b32 v1, a54
	v_accvgpr_read_b32 v4, a38
	v_cvt_pk_bf16_f32 v1, v4, v1
	v_lshl_add_u64 v[2:3], s[2:3], 0, v[2:3]
	global_store_dword v[2:3], v1, off
	v_or_b32_e32 v2, 11, v0
	v_ashrrev_i32_e32 v3, 31, v2
	v_lshlrev_b64 v[2:3], 7, v[2:3]
	v_accvgpr_read_b32 v1, a7
	v_accvgpr_read_b32 v4, a23
	v_or_b32_e32 v2, v2, v7
	v_cvt_pk_bf16_f32 v1, v4, v1
	v_lshl_add_u64 v[4:5], s[6:7], 0, v[2:3]
	global_store_dword v[4:5], v1, off
	v_accvgpr_read_b32 v1, a55
	v_accvgpr_read_b32 v4, a39
	v_cvt_pk_bf16_f32 v1, v4, v1
	v_lshl_add_u64 v[2:3], s[2:3], 0, v[2:3]
	global_store_dword v[2:3], v1, off
	v_or_b32_e32 v2, 16, v0
	v_ashrrev_i32_e32 v3, 31, v2
	v_lshlrev_b64 v[2:3], 7, v[2:3]
	v_accvgpr_read_b32 v1, a8
	v_accvgpr_read_b32 v4, a24
	v_or_b32_e32 v2, v2, v7
	v_cvt_pk_bf16_f32 v1, v4, v1
	v_lshl_add_u64 v[4:5], s[6:7], 0, v[2:3]
	global_store_dword v[4:5], v1, off
	v_accvgpr_read_b32 v1, a56
	v_accvgpr_read_b32 v4, a40
	v_cvt_pk_bf16_f32 v1, v4, v1
	v_lshl_add_u64 v[2:3], s[2:3], 0, v[2:3]
	global_store_dword v[2:3], v1, off
	v_or_b32_e32 v2, 17, v0
	v_ashrrev_i32_e32 v3, 31, v2
	v_lshlrev_b64 v[2:3], 7, v[2:3]
	v_accvgpr_read_b32 v1, a9
	v_accvgpr_read_b32 v4, a25
	v_or_b32_e32 v2, v2, v7
	v_cvt_pk_bf16_f32 v1, v4, v1
	v_lshl_add_u64 v[4:5], s[6:7], 0, v[2:3]
	global_store_dword v[4:5], v1, off
	v_accvgpr_read_b32 v1, a57
	v_accvgpr_read_b32 v4, a41
	v_cvt_pk_bf16_f32 v1, v4, v1
	v_lshl_add_u64 v[2:3], s[2:3], 0, v[2:3]
	global_store_dword v[2:3], v1, off
	v_or_b32_e32 v2, 18, v0
	v_ashrrev_i32_e32 v3, 31, v2
	v_lshlrev_b64 v[2:3], 7, v[2:3]
	v_accvgpr_read_b32 v1, a10
	v_accvgpr_read_b32 v4, a26
	v_or_b32_e32 v2, v2, v7
	v_cvt_pk_bf16_f32 v1, v4, v1
	v_lshl_add_u64 v[4:5], s[6:7], 0, v[2:3]
	global_store_dword v[4:5], v1, off
	v_accvgpr_read_b32 v1, a58
	v_accvgpr_read_b32 v4, a42
	v_cvt_pk_bf16_f32 v1, v4, v1
	v_lshl_add_u64 v[2:3], s[2:3], 0, v[2:3]
	global_store_dword v[2:3], v1, off
	v_or_b32_e32 v2, 19, v0
	v_ashrrev_i32_e32 v3, 31, v2
	v_lshlrev_b64 v[2:3], 7, v[2:3]
	v_accvgpr_read_b32 v1, a11
	v_accvgpr_read_b32 v4, a27
	v_or_b32_e32 v2, v2, v7
	v_cvt_pk_bf16_f32 v1, v4, v1
	v_lshl_add_u64 v[4:5], s[6:7], 0, v[2:3]
	global_store_dword v[4:5], v1, off
	v_accvgpr_read_b32 v1, a59
	v_accvgpr_read_b32 v4, a43
	v_cvt_pk_bf16_f32 v1, v4, v1
	v_lshl_add_u64 v[2:3], s[2:3], 0, v[2:3]
	global_store_dword v[2:3], v1, off
	v_or_b32_e32 v2, 24, v0
	v_ashrrev_i32_e32 v3, 31, v2
	v_lshlrev_b64 v[2:3], 7, v[2:3]
	v_accvgpr_read_b32 v1, a12
	v_accvgpr_read_b32 v4, a28
	v_or_b32_e32 v2, v2, v7
	v_cvt_pk_bf16_f32 v1, v4, v1
	v_lshl_add_u64 v[4:5], s[6:7], 0, v[2:3]
	global_store_dword v[4:5], v1, off
	v_accvgpr_read_b32 v1, a60
	v_accvgpr_read_b32 v4, a44
	v_cvt_pk_bf16_f32 v1, v4, v1
	v_lshl_add_u64 v[2:3], s[2:3], 0, v[2:3]
	global_store_dword v[2:3], v1, off
	v_or_b32_e32 v2, 25, v0
	v_ashrrev_i32_e32 v3, 31, v2
	v_lshlrev_b64 v[2:3], 7, v[2:3]
	v_accvgpr_read_b32 v1, a13
	v_accvgpr_read_b32 v4, a29
	v_or_b32_e32 v2, v2, v7
	v_cvt_pk_bf16_f32 v1, v4, v1
	v_lshl_add_u64 v[4:5], s[6:7], 0, v[2:3]
	global_store_dword v[4:5], v1, off
	v_accvgpr_read_b32 v1, a61
	v_accvgpr_read_b32 v4, a45
	v_cvt_pk_bf16_f32 v1, v4, v1
	v_lshl_add_u64 v[2:3], s[2:3], 0, v[2:3]
	global_store_dword v[2:3], v1, off
	v_or_b32_e32 v2, 26, v0
	v_ashrrev_i32_e32 v3, 31, v2
	v_lshlrev_b64 v[2:3], 7, v[2:3]
	v_accvgpr_read_b32 v1, a14
	v_accvgpr_read_b32 v4, a30
	v_or_b32_e32 v2, v2, v7
	v_cvt_pk_bf16_f32 v1, v4, v1
	v_lshl_add_u64 v[4:5], s[6:7], 0, v[2:3]
	global_store_dword v[4:5], v1, off
	v_accvgpr_read_b32 v1, a62
	v_accvgpr_read_b32 v4, a46
	v_cvt_pk_bf16_f32 v1, v4, v1
	v_lshl_add_u64 v[2:3], s[2:3], 0, v[2:3]
	v_or_b32_e32 v0, 27, v0
	global_store_dword v[2:3], v1, off
	v_ashrrev_i32_e32 v1, 31, v0
	v_lshlrev_b64 v[0:1], 7, v[0:1]
	v_accvgpr_read_b32 v2, a15
	v_accvgpr_read_b32 v3, a31
	v_or_b32_e32 v0, v0, v7
	v_cvt_pk_bf16_f32 v4, v3, v2
	v_lshl_add_u64 v[2:3], s[6:7], 0, v[0:1]
	global_store_dword v[2:3], v4, off
	v_accvgpr_read_b32 v2, a63
	v_accvgpr_read_b32 v3, a47
	v_cvt_pk_bf16_f32 v2, v3, v2
	v_lshl_add_u64 v[0:1], s[2:3], 0, v[0:1]
	global_store_dword v[0:1], v2, off
	s_branch .LBB5_84

	.amdhsa_kernel _Z14k_bcount_node0ItEvPKiPiS2_PKfS4_S4_S4_PK15HIP_vector_typeIjLj4EEPtPT_SB_
		.amdhsa_group_segment_fixed_size 45312
		.amdhsa_private_segment_fixed_size 0
		.amdhsa_kernarg_size 344
		.amdhsa_user_sgpr_count 2
		.amdhsa_user_sgpr_dispatch_ptr 0
		.amdhsa_user_sgpr_queue_ptr 0
		.amdhsa_user_sgpr_kernarg_segment_ptr 1
		.amdhsa_user_sgpr_dispatch_id 0
		.amdhsa_user_sgpr_kernarg_preload_length 0
		.amdhsa_user_sgpr_kernarg_preload_offset 0
		.amdhsa_user_sgpr_private_segment_size 0
		.amdhsa_uses_dynamic_stack 0
		.amdhsa_enable_private_segment 0
		.amdhsa_system_sgpr_workgroup_id_x 1
		.amdhsa_system_sgpr_workgroup_id_y 0
		.amdhsa_system_sgpr_workgroup_id_z 0
		.amdhsa_system_sgpr_workgroup_info 0
		.amdhsa_system_vgpr_workitem_id 0
		.amdhsa_next_free_vgpr 168
		.amdhsa_next_free_sgpr 96
		.amdhsa_accum_offset 104
		.amdhsa_reserve_vcc 1
		.amdhsa_float_round_mode_32 0
		.amdhsa_float_round_mode_16_64 0
		.amdhsa_float_denorm_mode_32 3
		.amdhsa_float_denorm_mode_16_64 3
		.amdhsa_dx10_clamp 1
		.amdhsa_ieee_mode 1
		.amdhsa_fp16_overflow 0
		.amdhsa_tg_split 0
		.amdhsa_exception_fp_ieee_invalid_op 0
		.amdhsa_exception_fp_denorm_src 0
		.amdhsa_exception_fp_ieee_div_zero 0
		.amdhsa_exception_fp_ieee_overflow 0
		.amdhsa_exception_fp_ieee_underflow 0
		.amdhsa_exception_fp_ieee_inexact 0
		.amdhsa_exception_int_div_zero 0
	.end_amdhsa_kernel

amdhsa.kernels:
  - .agpr_count:     0
    .args:
      - .actual_access:  read_only
        .address_space:  global
        .offset:         0
        .size:           8
        .value_kind:     global_buffer
      - .actual_access:  read_only
        .address_space:  global
        .offset:         8
        .size:           8
        .value_kind:     global_buffer
      - .actual_access:  read_only
        .address_space:  global
        .offset:         16
        .size:           8
        .value_kind:     global_buffer
      - .actual_access:  read_only
        .address_space:  global
        .offset:         24
        .size:           8
        .value_kind:     global_buffer
      - .actual_access:  write_only
        .address_space:  global
        .offset:         32
        .size:           8
        .value_kind:     global_buffer
      - .actual_access:  write_only
        .address_space:  global
        .offset:         40
        .size:           8
        .value_kind:     global_buffer
      - .actual_access:  write_only
        .address_space:  global
        .offset:         48
        .size:           8
        .value_kind:     global_buffer
      - .offset:         56
        .size:           4
        .value_kind:     hidden_block_count_x
      - .offset:         60
        .size:           4
        .value_kind:     hidden_block_count_y
      - .offset:         64
        .size:           4
        .value_kind:     hidden_block_count_z
      - .offset:         68
        .size:           2
        .value_kind:     hidden_group_size_x
      - .offset:         70
        .size:           2
        .value_kind:     hidden_group_size_y
      - .offset:         72
        .size:           2
        .value_kind:     hidden_group_size_z
      - .offset:         74
        .size:           2
        .value_kind:     hidden_remainder_x
      - .offset:         76
        .size:           2
        .value_kind:     hidden_remainder_y
      - .offset:         78
        .size:           2
        .value_kind:     hidden_remainder_z
      - .offset:         96
        .size:           8
        .value_kind:     hidden_global_offset_x
      - .offset:         104
        .size:           8
        .value_kind:     hidden_global_offset_y
      - .offset:         112
        .size:           8
        .value_kind:     hidden_global_offset_z
      - .offset:         120
        .size:           2
        .value_kind:     hidden_grid_dims
    .group_segment_fixed_size: 0
    .kernarg_segment_align: 8
    .kernarg_segment_size: 312
    .language:       OpenCL C
    .language_version:
      - 2
      - 0
    .max_flat_workgroup_size: 256
    .name:           _Z6k_prepPKfS0_S0_S0_P15HIP_vector_typeIjLj4EEPiPd
    .private_segment_fixed_size: 0
    .sgpr_count:     25
    .sgpr_spill_count: 0
    .symbol:         _Z6k_prepPKfS0_S0_S0_P15HIP_vector_typeIjLj4EEPiPd.kd
    .uniform_work_group_size: 1
    .uses_dynamic_stack: false
    .vgpr_count:     24
    .vgpr_spill_count: 0
    .wavefront_size: 64
  - .agpr_count:     0
    .args:
      - .actual_access:  read_only
        .address_space:  global
        .offset:         0
        .size:           8
        .value_kind:     global_buffer
      - .actual_access:  read_only
        .address_space:  global
        .offset:         8
        .size:           8
        .value_kind:     global_buffer
      - .actual_access:  read_only
        .address_space:  global
        .offset:         16
        .size:           8
        .value_kind:     global_buffer
      - .actual_access:  read_only
        .address_space:  global
        .offset:         24
        .size:           8
        .value_kind:     global_buffer
      - .actual_access:  read_only
        .address_space:  global
        .offset:         32
        .size:           8
        .value_kind:     global_buffer
      - .actual_access:  write_only
        .address_space:  global
        .offset:         40
        .size:           8
        .value_kind:     global_buffer
      - .actual_access:  write_only
        .address_space:  global
        .offset:         48
        .size:           8
        .value_kind:     global_buffer
    .group_segment_fixed_size: 4112
    .kernarg_segment_align: 8
    .kernarg_segment_size: 56
    .language:       OpenCL C
    .language_version:
      - 2
      - 0
    .max_flat_workgroup_size: 256
    .name:           _Z10k_bscatterPKiS0_PKfS0_S0_PiP15HIP_vector_typeIjLj2EE
    .private_segment_fixed_size: 0
    .sgpr_count:     28
    .sgpr_spill_count: 0
    .symbol:         _Z10k_bscatterPKiS0_PKfS0_S0_PiP15HIP_vector_typeIjLj2EE.kd
    .uniform_work_group_size: 1
    .uses_dynamic_stack: false
    .vgpr_count:     78
    .vgpr_spill_count: 0
    .wavefront_size: 64
  - .agpr_count:     0
    .args:
      - .actual_access:  read_only
        .address_space:  global
        .offset:         0
        .size:           8
        .value_kind:     global_buffer
      - .actual_access:  read_only
        .address_space:  global
        .offset:         8
        .size:           8
        .value_kind:     global_buffer
      - .actual_access:  write_only
        .address_space:  global
        .offset:         16
        .size:           8
        .value_kind:     global_buffer
      - .actual_access:  write_only
        .address_space:  global
        .offset:         24
        .size:           8
        .value_kind:     global_buffer
      - .actual_access:  write_only
        .address_space:  global
        .offset:         32
        .size:           8
        .value_kind:     global_buffer
      - .actual_access:  write_only
        .address_space:  global
        .offset:         40
        .size:           8
        .value_kind:     global_buffer
    .group_segment_fixed_size: 29200
    .kernarg_segment_align: 8
    .kernarg_segment_size: 48
    .language:       OpenCL C
    .language_version:
      - 2
      - 0
    .max_flat_workgroup_size: 256
    .name:           _Z7k_bsortPKiPK15HIP_vector_typeIjLj2EEPiS5_S5_Pf
    .private_segment_fixed_size: 0
    .sgpr_count:     106
    .sgpr_spill_count: 12
    .symbol:         _Z7k_bsortPKiPK15HIP_vector_typeIjLj2EEPiS5_S5_Pf.kd
    .uniform_work_group_size: 1
    .uses_dynamic_stack: false
    .vgpr_count:     69
    .vgpr_spill_count: 0
    .wavefront_size: 64
  - .agpr_count:     32
    .args:
      - .address_space:  global
        .offset:         0
        .size:           8
        .value_kind:     global_buffer
      - .actual_access:  read_only
        .address_space:  global
        .offset:         8
        .size:           8
        .value_kind:     global_buffer
      - .actual_access:  read_only
        .address_space:  global
        .offset:         16
        .size:           8
        .value_kind:     global_buffer
      - .actual_access:  read_only
        .address_space:  global
        .offset:         24
        .size:           8
        .value_kind:     global_buffer
      - .actual_access:  read_only
        .address_space:  global
        .offset:         32
        .size:           8
        .value_kind:     global_buffer
      - .actual_access:  read_only
        .address_space:  global
        .offset:         40
        .size:           8
        .value_kind:     global_buffer
      - .address_space:  global
        .offset:         48
        .size:           8
        .value_kind:     global_buffer
      - .address_space:  global
        .offset:         56
        .size:           8
        .value_kind:     global_buffer
      - .offset:         64
        .size:           4
        .value_kind:     hidden_block_count_x
      - .offset:         68
        .size:           4
        .value_kind:     hidden_block_count_y
      - .offset:         72
        .size:           4
        .value_kind:     hidden_block_count_z
      - .offset:         76
        .size:           2
        .value_kind:     hidden_group_size_x
      - .offset:         78
        .size:           2
        .value_kind:     hidden_group_size_y
      - .offset:         80
        .size:           2
        .value_kind:     hidden_group_size_z
      - .offset:         82
        .size:           2
        .value_kind:     hidden_remainder_x
      - .offset:         84
        .size:           2
        .value_kind:     hidden_remainder_y
      - .offset:         86
        .size:           2
        .value_kind:     hidden_remainder_z
      - .offset:         104
        .size:           8
        .value_kind:     hidden_global_offset_x
      - .offset:         112
        .size:           8
        .value_kind:     hidden_global_offset_y
      - .offset:         120
        .size:           8
        .value_kind:     hidden_global_offset_z
      - .offset:         128
        .size:           2
        .value_kind:     hidden_grid_dims
    .group_segment_fixed_size: 18944
    .kernarg_segment_align: 8
    .kernarg_segment_size: 320
    .language:       OpenCL C
    .language_version:
      - 2
      - 0
    .max_flat_workgroup_size: 256
    .name:           _Z4k_U2PKtPK15HIP_vector_typeIjLj4EEPKdPKfS8_S8_PtPd
    .private_segment_fixed_size: 0
    .sgpr_count:     34
    .sgpr_spill_count: 0
    .symbol:         _Z4k_U2PKtPK15HIP_vector_typeIjLj4EEPKdPKfS8_S8_PtPd.kd
    .uniform_work_group_size: 1
    .uses_dynamic_stack: false
    .vgpr_count:     104
    .vgpr_spill_count: 0
    .wavefront_size: 64
  - .agpr_count:     0
    .args:
      - .actual_access:  read_only
        .address_space:  global
        .offset:         0
        .size:           8
        .value_kind:     global_buffer
      - .actual_access:  read_only
        .address_space:  global
        .offset:         8
        .size:           8
        .value_kind:     global_buffer
      - .actual_access:  write_only
        .address_space:  global
        .offset:         16
        .size:           8
        .value_kind:     global_buffer
    .group_segment_fixed_size: 0
    .kernarg_segment_align: 8
    .kernarg_segment_size: 24
    .language:       OpenCL C
    .language_version:
      - 2
      - 0
    .max_flat_workgroup_size: 1024
    .name:           _Z7k_finalPKdPKfPf
    .private_segment_fixed_size: 0
    .sgpr_count:     28
    .sgpr_spill_count: 0
    .symbol:         _Z7k_finalPKdPKfPf.kd
    .uniform_work_group_size: 1
    .uses_dynamic_stack: false
    .vgpr_count:     10
    .vgpr_spill_count: 0
    .wavefront_size: 64
  - .agpr_count:     64
    .args:
      - .actual_access:  read_only
        .address_space:  global
        .offset:         0
        .size:           8
        .value_kind:     global_buffer
      - .address_space:  global
        .offset:         8
        .size:           8
        .value_kind:     global_buffer
      - .actual_access:  write_only
        .address_space:  global
        .offset:         16
        .size:           8
        .value_kind:     global_buffer
      - .actual_access:  read_only
        .address_space:  global
        .offset:         24
        .size:           8
        .value_kind:     global_buffer
      - .actual_access:  read_only
        .address_space:  global
        .offset:         32
        .size:           8
        .value_kind:     global_buffer
      - .actual_access:  read_only
        .address_space:  global
        .offset:         40
        .size:           8
        .value_kind:     global_buffer
      - .actual_access:  read_only
        .address_space:  global
        .offset:         48
        .size:           8
        .value_kind:     global_buffer
      - .actual_access:  read_only
        .address_space:  global
        .offset:         56
        .size:           8
        .value_kind:     global_buffer
      - .actual_access:  write_only
        .address_space:  global
        .offset:         64
        .size:           8
        .value_kind:     global_buffer
      - .actual_access:  write_only
        .address_space:  global
        .offset:         72
        .size:           8
        .value_kind:     global_buffer
      - .actual_access:  write_only
        .address_space:  global
        .offset:         80
        .size:           8
        .value_kind:     global_buffer
      - .offset:         88
        .size:           4
        .value_kind:     hidden_block_count_x
      - .offset:         92
        .size:           4
        .value_kind:     hidden_block_count_y
      - .offset:         96
        .size:           4
        .value_kind:     hidden_block_count_z
      - .offset:         100
        .size:           2
        .value_kind:     hidden_group_size_x
      - .offset:         102
        .size:           2
        .value_kind:     hidden_group_size_y
      - .offset:         104
        .size:           2
        .value_kind:     hidden_group_size_z
      - .offset:         106
        .size:           2
        .value_kind:     hidden_remainder_x
      - .offset:         108
        .size:           2
        .value_kind:     hidden_remainder_y
      - .offset:         110
        .size:           2
        .value_kind:     hidden_remainder_z
      - .offset:         128
        .size:           8
        .value_kind:     hidden_global_offset_x
      - .offset:         136
        .size:           8
        .value_kind:     hidden_global_offset_y
      - .offset:         144
        .size:           8
        .value_kind:     hidden_global_offset_z
      - .offset:         152
        .size:           2
        .value_kind:     hidden_grid_dims
    .group_segment_fixed_size: 45312
    .kernarg_segment_align: 8
    .kernarg_segment_size: 344
    .language:       OpenCL C
    .language_version:
      - 2
      - 0
    .max_flat_workgroup_size: 256
    .name:           _Z14k_bcount_node0ItEvPKiPiS2_PKfS4_S4_S4_PK15HIP_vector_typeIjLj4EEPtPT_SB_
    .private_segment_fixed_size: 0
    .sgpr_count:     26
    .sgpr_spill_count: 0
    .symbol:         _Z14k_bcount_node0ItEvPKiPiS2_PKfS4_S4_S4_PK15HIP_vector_typeIjLj4EEPtPT_SB_.kd
    .uniform_work_group_size: 1
    .uses_dynamic_stack: false
    .vgpr_count:     104
    .vgpr_spill_count: 0
    .wavefront_size: 64
  - .agpr_count:     0
    .args:
      - .actual_access:  read_only
        .address_space:  global
        .offset:         0
        .size:           8
        .value_kind:     global_buffer
      - .actual_access:  read_only
        .address_space:  global
        .offset:         8
        .size:           8
        .value_kind:     global_buffer
      - .actual_access:  read_only
        .address_space:  global
        .offset:         16
        .size:           8
        .value_kind:     global_buffer
      - .actual_access:  read_only
        .address_space:  global
        .offset:         24
        .size:           8
        .value_kind:     global_buffer
      - .actual_access:  read_only
        .address_space:  global
        .offset:         32
        .size:           8
        .value_kind:     global_buffer
      - .actual_access:  read_only
        .address_space:  global
        .offset:         40
        .size:           8
        .value_kind:     global_buffer
      - .address_space:  global
        .offset:         48
        .size:           8
        .value_kind:     global_buffer
      - .offset:         56
        .size:           4
        .value_kind:     hidden_block_count_x
      - .offset:         60
        .size:           4
        .value_kind:     hidden_block_count_y
      - .offset:         64
        .size:           4
        .value_kind:     hidden_block_count_z
      - .offset:         68
        .size:           2
        .value_kind:     hidden_group_size_x
      - .offset:         70
        .size:           2
        .value_kind:     hidden_group_size_y
      - .offset:         72
        .size:           2
        .value_kind:     hidden_group_size_z
      - .offset:         74
        .size:           2
        .value_kind:     hidden_remainder_x
      - .offset:         76
        .size:           2
        .value_kind:     hidden_remainder_y
      - .offset:         78
        .size:           2
        .value_kind:     hidden_remainder_z
      - .offset:         96
        .size:           8
        .value_kind:     hidden_global_offset_x
      - .offset:         104
        .size:           8
        .value_kind:     hidden_global_offset_y
      - .offset:         112
        .size:           8
        .value_kind:     hidden_global_offset_z
      - .offset:         120
        .size:           2
        .value_kind:     hidden_grid_dims
    .group_segment_fixed_size: 2048
    .kernarg_segment_align: 8
    .kernarg_segment_size: 312
    .language:       OpenCL C
    .language_version:
      - 2
      - 0
    .max_flat_workgroup_size: 256
    .name:           _Z7k_passAItEvPKiS1_PKfPKT_S6_S3_Pd
    .private_segment_fixed_size: 0
    .sgpr_count:     36
    .sgpr_spill_count: 0
    .symbol:         _Z7k_passAItEvPKiS1_PKfPKT_S6_S3_Pd.kd
    .uniform_work_group_size: 1
    .uses_dynamic_stack: false
    .vgpr_count:     104
    .vgpr_spill_count: 0
    .wavefront_size: 64
  - .agpr_count:     0
    .args:
      - .actual_access:  read_only
        .address_space:  global
        .offset:         0
        .size:           8
        .value_kind:     global_buffer
      - .actual_access:  read_only
        .address_space:  global
        .offset:         8
        .size:           8
        .value_kind:     global_buffer
      - .actual_access:  read_only
        .address_space:  global
        .offset:         16
        .size:           8
        .value_kind:     global_buffer
      - .actual_access:  read_only
        .address_space:  global
        .offset:         24
        .size:           8
        .value_kind:     global_buffer
      - .actual_access:  read_only
        .address_space:  global
        .offset:         32
        .size:           8
        .value_kind:     global_buffer
      - .actual_access:  read_only
        .address_space:  global
        .offset:         40
        .size:           8
        .value_kind:     global_buffer
      - .actual_access:  read_only
        .address_space:  global
        .offset:         48
        .size:           8
        .value_kind:     global_buffer
      - .actual_access:  read_only
        .address_space:  global
        .offset:         56
        .size:           8
        .value_kind:     global_buffer
      - .actual_access:  read_only
        .address_space:  global
        .offset:         64
        .size:           8
        .value_kind:     global_buffer
      - .actual_access:  read_only
        .address_space:  global
        .offset:         72
        .size:           8
        .value_kind:     global_buffer
      - .actual_access:  read_only
        .address_space:  global
        .offset:         80
        .size:           8
        .value_kind:     global_buffer
      - .actual_access:  read_only
        .address_space:  global
        .offset:         88
        .size:           8
        .value_kind:     global_buffer
      - .actual_access:  read_only
        .address_space:  global
        .offset:         96
        .size:           8
        .value_kind:     global_buffer
      - .address_space:  global
        .offset:         104
        .size:           8
        .value_kind:     global_buffer
      - .actual_access:  read_only
        .address_space:  global
        .offset:         112
        .size:           8
        .value_kind:     global_buffer
      - .actual_access:  read_only
        .address_space:  global
        .offset:         120
        .size:           8
        .value_kind:     global_buffer
      - .address_space:  global
        .offset:         128
        .size:           8
        .value_kind:     global_buffer
      - .offset:         136
        .size:           4
        .value_kind:     hidden_block_count_x
      - .offset:         140
        .size:           4
        .value_kind:     hidden_block_count_y
      - .offset:         144
        .size:           4
        .value_kind:     hidden_block_count_z
      - .offset:         148
        .size:           2
        .value_kind:     hidden_group_size_x
      - .offset:         150
        .size:           2
        .value_kind:     hidden_group_size_y
      - .offset:         152
        .size:           2
        .value_kind:     hidden_group_size_z
      - .offset:         154
        .size:           2
        .value_kind:     hidden_remainder_x
      - .offset:         156
        .size:           2
        .value_kind:     hidden_remainder_y
      - .offset:         158
        .size:           2
        .value_kind:     hidden_remainder_z
      - .offset:         176
        .size:           8
        .value_kind:     hidden_global_offset_x
      - .offset:         184
        .size:           8
        .value_kind:     hidden_global_offset_y
      - .offset:         192
        .size:           8
        .value_kind:     hidden_global_offset_z
      - .offset:         200
        .size:           2
        .value_kind:     hidden_grid_dims
    .group_segment_fixed_size: 37632
    .kernarg_segment_align: 8
    .kernarg_segment_size: 392
    .language:       OpenCL C
    .language_version:
      - 2
      - 0
    .max_flat_workgroup_size: 256
    .name:           _Z7k_passLILi1ELi0ELi1EEvPKiS1_PKfPKtS5_S3_S3_S3_S3_S3_S3_PK15HIP_vector_typeIjLj4EEPKdPdS1_PtS1_
    .private_segment_fixed_size: 0
    .sgpr_count:     62
    .sgpr_spill_count: 0
    .symbol:         _Z7k_passLILi1ELi0ELi1EEvPKiS1_PKfPKtS5_S3_S3_S3_S3_S3_S3_PK15HIP_vector_typeIjLj4EEPKdPdS1_PtS1_.kd
    .uniform_work_group_size: 1
    .uses_dynamic_stack: false
    .vgpr_count:     128
    .vgpr_spill_count: 0
    .wavefront_size: 64
  - .agpr_count:     0
    .args:
      - .actual_access:  read_only
        .address_space:  global
        .offset:         0
        .size:           8
        .value_kind:     global_buffer
      - .actual_access:  read_only
        .address_space:  global
        .offset:         8
        .size:           8
        .value_kind:     global_buffer
      - .actual_access:  read_only
        .address_space:  global
        .offset:         16
        .size:           8
        .value_kind:     global_buffer
      - .actual_access:  read_only
        .address_space:  global
        .offset:         24
        .size:           8
        .value_kind:     global_buffer
      - .actual_access:  read_only
        .address_space:  global
        .offset:         32
        .size:           8
        .value_kind:     global_buffer
      - .actual_access:  read_only
        .address_space:  global
        .offset:         40
        .size:           8
        .value_kind:     global_buffer
      - .actual_access:  read_only
        .address_space:  global
        .offset:         48
        .size:           8
        .value_kind:     global_buffer
      - .actual_access:  read_only
        .address_space:  global
        .offset:         56
        .size:           8
        .value_kind:     global_buffer
      - .actual_access:  read_only
        .address_space:  global
        .offset:         64
        .size:           8
        .value_kind:     global_buffer
      - .actual_access:  read_only
        .address_space:  global
        .offset:         72
        .size:           8
        .value_kind:     global_buffer
      - .actual_access:  read_only
        .address_space:  global
        .offset:         80
        .size:           8
        .value_kind:     global_buffer
      - .actual_access:  read_only
        .address_space:  global
        .offset:         88
        .size:           8
        .value_kind:     global_buffer
      - .actual_access:  read_only
        .address_space:  global
        .offset:         96
        .size:           8
        .value_kind:     global_buffer
      - .actual_access:  read_only
        .address_space:  global
        .offset:         104
        .size:           8
        .value_kind:     global_buffer
      - .actual_access:  read_only
        .address_space:  global
        .offset:         112
        .size:           8
        .value_kind:     global_buffer
      - .actual_access:  read_only
        .address_space:  global
        .offset:         120
        .size:           8
        .value_kind:     global_buffer
      - .actual_access:  read_only
        .address_space:  global
        .offset:         128
        .size:           8
        .value_kind:     global_buffer
      - .address_space:  global
        .offset:         136
        .size:           8
        .value_kind:     global_buffer
      - .actual_access:  read_only
        .address_space:  global
        .offset:         144
        .size:           8
        .value_kind:     global_buffer
      - .actual_access:  read_only
        .address_space:  global
        .offset:         152
        .size:           8
        .value_kind:     global_buffer
      - .actual_access:  write_only
        .address_space:  global
        .offset:         160
        .size:           8
        .value_kind:     global_buffer
      - .address_space:  global
        .offset:         168
        .size:           8
        .value_kind:     global_buffer
      - .offset:         176
        .size:           4
        .value_kind:     hidden_block_count_x
      - .offset:         180
        .size:           4
        .value_kind:     hidden_block_count_y
      - .offset:         184
        .size:           4
        .value_kind:     hidden_block_count_z
      - .offset:         188
        .size:           2
        .value_kind:     hidden_group_size_x
      - .offset:         190
        .size:           2
        .value_kind:     hidden_group_size_y
      - .offset:         192
        .size:           2
        .value_kind:     hidden_group_size_z
      - .offset:         194
        .size:           2
        .value_kind:     hidden_remainder_x
      - .offset:         196
        .size:           2
        .value_kind:     hidden_remainder_y
      - .offset:         198
        .size:           2
        .value_kind:     hidden_remainder_z
      - .offset:         216
        .size:           8
        .value_kind:     hidden_global_offset_x
      - .offset:         224
        .size:           8
        .value_kind:     hidden_global_offset_y
      - .offset:         232
        .size:           8
        .value_kind:     hidden_global_offset_z
      - .offset:         240
        .size:           2
        .value_kind:     hidden_grid_dims
    .group_segment_fixed_size: 79104
    .kernarg_segment_align: 8
    .kernarg_segment_size: 432
    .language:       OpenCL C
    .language_version:
      - 2
      - 0
    .max_flat_workgroup_size: 512
    .name:           _Z8k_passCUILi1EEvPKiS1_PKfPKtS5_S3_S3_S3_S3_S3_S3_PK15HIP_vector_typeIjLj4EES9_S9_PKdSB_S1_S1_S5_S3_PtPd
    .private_segment_fixed_size: 0
    .sgpr_count:     35
    .sgpr_spill_count: 0
    .symbol:         _Z8k_passCUILi1EEvPKiS1_PKfPKtS5_S3_S3_S3_S3_S3_S3_PK15HIP_vector_typeIjLj4EES9_S9_PKdSB_S1_S1_S5_S3_PtPd.kd
    .uniform_work_group_size: 1
    .uses_dynamic_stack: false
    .vgpr_count:     128
    .vgpr_spill_count: 0
    .wavefront_size: 64
  - .agpr_count:     64
    .args:
      - .actual_access:  read_only
        .address_space:  global
        .offset:         0
        .size:           8
        .value_kind:     global_buffer
      - .address_space:  global
        .offset:         8
        .size:           8
        .value_kind:     global_buffer
      - .actual_access:  read_only
        .address_space:  global
        .offset:         16
        .size:           8
        .value_kind:     global_buffer
      - .actual_access:  read_only
        .address_space:  global
        .offset:         24
        .size:           8
        .value_kind:     global_buffer
      - .actual_access:  read_only
        .address_space:  global
        .offset:         32
        .size:           8
        .value_kind:     global_buffer
      - .actual_access:  read_only
        .address_space:  global
        .offset:         40
        .size:           8
        .value_kind:     global_buffer
      - .actual_access:  read_only
        .address_space:  global
        .offset:         48
        .size:           8
        .value_kind:     global_buffer
      - .actual_access:  write_only
        .address_space:  global
        .offset:         56
        .size:           8
        .value_kind:     global_buffer
      - .actual_access:  write_only
        .address_space:  global
        .offset:         64
        .size:           8
        .value_kind:     global_buffer
      - .actual_access:  read_only
        .address_space:  global
        .offset:         72
        .size:           8
        .value_kind:     global_buffer
      - .actual_access:  read_only
        .address_space:  global
        .offset:         80
        .size:           8
        .value_kind:     global_buffer
      - .offset:         88
        .size:           4
        .value_kind:     hidden_block_count_x
      - .offset:         92
        .size:           4
        .value_kind:     hidden_block_count_y
      - .offset:         96
        .size:           4
        .value_kind:     hidden_block_count_z
      - .offset:         100
        .size:           2
        .value_kind:     hidden_group_size_x
      - .offset:         102
        .size:           2
        .value_kind:     hidden_group_size_y
      - .offset:         104
        .size:           2
        .value_kind:     hidden_group_size_z
      - .offset:         106
        .size:           2
        .value_kind:     hidden_remainder_x
      - .offset:         108
        .size:           2
        .value_kind:     hidden_remainder_y
      - .offset:         110
        .size:           2
        .value_kind:     hidden_remainder_z
      - .offset:         128
        .size:           8
        .value_kind:     hidden_global_offset_x
      - .offset:         136
        .size:           8
        .value_kind:     hidden_global_offset_y
      - .offset:         144
        .size:           8
        .value_kind:     hidden_global_offset_z
      - .offset:         152
        .size:           2
        .value_kind:     hidden_grid_dims
    .group_segment_fixed_size: 33280
    .kernarg_segment_align: 8
    .kernarg_segment_size: 344
    .language:       OpenCL C
    .language_version:
      - 2
      - 0
    .max_flat_workgroup_size: 256
    .name:           _Z4k_U3ILb0EtEvPKtPtPKdPKfS6_PK15HIP_vector_typeIjLj4EES6_PT0_SC_S6_Pd
    .private_segment_fixed_size: 0
    .sgpr_count:     20
    .sgpr_spill_count: 0
    .symbol:         _Z4k_U3ILb0EtEvPKtPtPKdPKfS6_PK15HIP_vector_typeIjLj4EES6_PT0_SC_S6_Pd.kd
    .uniform_work_group_size: 1
    .uses_dynamic_stack: false
    .vgpr_count:     144
    .vgpr_spill_count: 0
    .wavefront_size: 64
  - .agpr_count:     0
    .args:
      - .actual_access:  read_only
        .address_space:  global
        .offset:         0
        .size:           8
        .value_kind:     global_buffer
      - .actual_access:  read_only
        .address_space:  global
        .offset:         8
        .size:           8
        .value_kind:     global_buffer
      - .actual_access:  read_only
        .address_space:  global
        .offset:         16
        .size:           8
        .value_kind:     global_buffer
      - .actual_access:  read_only
        .address_space:  global
        .offset:         24
        .size:           8
        .value_kind:     global_buffer
      - .actual_access:  read_only
        .address_space:  global
        .offset:         32
        .size:           8
        .value_kind:     global_buffer
      - .actual_access:  read_only
        .address_space:  global
        .offset:         40
        .size:           8
        .value_kind:     global_buffer
      - .actual_access:  read_only
        .address_space:  global
        .offset:         48
        .size:           8
        .value_kind:     global_buffer
      - .actual_access:  read_only
        .address_space:  global
        .offset:         56
        .size:           8
        .value_kind:     global_buffer
      - .actual_access:  read_only
        .address_space:  global
        .offset:         64
        .size:           8
        .value_kind:     global_buffer
      - .actual_access:  read_only
        .address_space:  global
        .offset:         72
        .size:           8
        .value_kind:     global_buffer
      - .address_space:  global
        .offset:         80
        .size:           8
        .value_kind:     global_buffer
      - .offset:         88
        .size:           4
        .value_kind:     hidden_block_count_x
      - .offset:         92
        .size:           4
        .value_kind:     hidden_block_count_y
      - .offset:         96
        .size:           4
        .value_kind:     hidden_block_count_z
      - .offset:         100
        .size:           2
        .value_kind:     hidden_group_size_x
      - .offset:         102
        .size:           2
        .value_kind:     hidden_group_size_y
      - .offset:         104
        .size:           2
        .value_kind:     hidden_group_size_z
      - .offset:         106
        .size:           2
        .value_kind:     hidden_remainder_x
      - .offset:         108
        .size:           2
        .value_kind:     hidden_remainder_y
      - .offset:         110
        .size:           2
        .value_kind:     hidden_remainder_z
      - .offset:         128
        .size:           8
        .value_kind:     hidden_global_offset_x
      - .offset:         136
        .size:           8
        .value_kind:     hidden_global_offset_y
      - .offset:         144
        .size:           8
        .value_kind:     hidden_global_offset_z
      - .offset:         152
        .size:           2
        .value_kind:     hidden_grid_dims
    .group_segment_fixed_size: 784
    .kernarg_segment_align: 8
    .kernarg_segment_size: 344
    .language:       OpenCL C
    .language_version:
      - 2
      - 0
    .max_flat_workgroup_size: 256
    .name:           _Z4k_U3ILb1EtEvPKtPtPKdPKfS6_PK15HIP_vector_typeIjLj4EES6_PT0_SC_S6_Pd
    .private_segment_fixed_size: 0
    .sgpr_count:     20
    .sgpr_spill_count: 0
    .symbol:         _Z4k_U3ILb1EtEvPKtPtPKdPKfS6_PK15HIP_vector_typeIjLj4EES6_PT0_SC_S6_Pd.kd
    .uniform_work_group_size: 1
    .uses_dynamic_stack: false
    .vgpr_count:     79
    .vgpr_spill_count: 0
    .wavefront_size: 64
